# speedup vs baseline: 1.0039x; 1.0039x over previous
.LBB2_3:
	s_add_i32 s19, s15, s19
	s_cmpk_lt_i32 s19, 0x61b
	s_cselect_b64 s[8:9], -1, 0
	s_cmpk_gt_i32 s19, 0x61a
	s_cselect_b64 s[0:1], -1, 0
	s_and_b64 vcc, exec, s[0:1]
	s_cbranch_vccnz .LBB2_5
	v_add_u32_e32 v60, s14, v215
	v_min_i32_e32 v34, 0xc34f, v60
	v_add_u32_e32 v36, 8, v60
	v_add_u32_e32 v58, 16, v60
	v_add_u32_e32 v60, 24, v60
	v_min_i32_e32 v36, 0xc34f, v36
	v_min_i32_e32 v58, 0xc34f, v58
	v_min_i32_e32 v60, 0xc34f, v60
	v_ashrrev_i32_e32 v35, 31, v34
	v_ashrrev_i32_e32 v37, 31, v36
	v_ashrrev_i32_e32 v59, 31, v58
	v_ashrrev_i32_e32 v61, 31, v60
	v_lshlrev_b64 v[34:35], 9, v[34:35]
	v_lshlrev_b64 v[36:37], 9, v[36:37]
	v_lshlrev_b64 v[58:59], 9, v[58:59]
	v_lshlrev_b64 v[60:61], 9, v[60:61]
	v_lshl_add_u64 v[34:35], v[210:211], 0, v[34:35]
	v_lshl_add_u64 v[38:39], v[210:211], 0, v[36:37]
	v_lshl_add_u64 v[58:59], v[210:211], 0, v[58:59]
	v_lshl_add_u64 v[70:71], v[210:211], 0, v[60:61]
	global_load_dwordx4 v[34:37], v[34:35], off nt
	s_nop 0
	global_load_dwordx4 v[38:41], v[38:39], off nt
	s_nop 0
	global_load_dwordx4 v[58:61], v[58:59], off nt
	s_nop 0
	global_load_dwordx4 v[70:73], v[70:71], off nt

.LBB2_9:
	s_or_b64 exec, exec, s[10:11]
	s_andn2_b64 vcc, exec, s[8:9]
	s_xor_b32 s20, s20, 1
	s_cbranch_vccnz .LBB2_2
	s_mul_i32 s8, s20, 0x4200
	v_add_u32_e32 v178, s8, v213
	s_waitcnt vmcnt(7)
	ds_write_b128 v178, v[34:37]
	s_waitcnt vmcnt(6)
	ds_write_b128 v178, v[38:41] offset:4224
	s_waitcnt vmcnt(5)
	ds_write_b128 v178, v[58:61] offset:8448
	s_waitcnt vmcnt(4)
	ds_write_b128 v178, v[70:73] offset:12672
	s_branch .LBB2_2

.LBB2_14:
	s_or_b64 exec, exec, s[0:1]
	v_lshlrev_b32_e32 v0, 2, v0
	s_waitcnt lgkmcnt(0)
	s_barrier
	ds_read_b32 v1, v0
	s_lshl_b32 s0, s2, 11
	s_and_b32 s0, s0, 0x3800
	s_add_u32 s0, s12, s0
	s_addc_u32 s1, s13, 0
	s_waitcnt lgkmcnt(0)
	global_atomic_add_f32 v0, v1, s[0:1]
	ds_read_b32 v1, v0 offset:1024
	s_waitcnt lgkmcnt(0)
	global_atomic_add_f32 v0, v1, s[0:1] offset:1024
	s_endpgm
	.p2alignl 8, 3212836864

_Z11gemm_kernelILi2EEvPKDF16_S1_PKfPDF16_PfS5_S3_S3_S1_S3_:
	s_load_dwordx4 s[8:11], s[0:1], 0x28
	s_load_dwordx4 s[4:7], s[0:1], 0x0
	v_mov_b32_e32 v211, 0
	v_lshlrev_b32_e32 v178, 2, v0
	v_mov_b32_e32 v179, v211
	s_waitcnt lgkmcnt(0)
	v_lshl_add_u64 v[2:3], s[8:9], 0, v[178:179]
	s_movk_i32 s3, 0x1000
	v_add_co_u32_e32 v4, vcc, s3, v2
	s_movk_i32 s14, 0x2000
	s_nop 0
	v_addc_co_u32_e32 v5, vcc, 0, v3, vcc
	v_add_co_u32_e32 v6, vcc, s14, v2
	s_movk_i32 s15, 0x3000
	s_nop 0
	v_addc_co_u32_e32 v7, vcc, 0, v3, vcc
	global_load_dword v36, v178, s[8:9]
	global_load_dword v37, v178, s[8:9] offset:1024
	global_load_dword v38, v178, s[8:9] offset:2048
	global_load_dword v39, v178, s[8:9] offset:3072
	global_load_dword v40, v[6:7], off offset:-4096
	global_load_dword v41, v[4:5], off offset:1024
	global_load_dword v44, v[4:5], off offset:2048
	global_load_dword v45, v[4:5], off offset:3072
	global_load_dword v46, v[6:7], off
	global_load_dword v47, v[6:7], off offset:1024
	global_load_dword v48, v[6:7], off offset:2048
	global_load_dword v49, v[6:7], off offset:3072
	v_add_co_u32_e32 v2, vcc, s15, v2
	v_lshrrev_b32_e32 v1, 6, v0
	s_nop 0
	v_addc_co_u32_e32 v3, vcc, 0, v3, vcc
	global_load_dword v50, v[2:3], off
	global_load_dword v51, v[2:3], off offset:1024
	global_load_dword v52, v[2:3], off offset:2048
	global_load_dword v53, v[2:3], off offset:3072
	s_load_dwordx2 s[8:9], s[0:1], 0x48
	s_load_dwordx2 s[12:13], s[0:1], 0x38
	global_load_dword v54, v178, s[10:11]
	s_waitcnt lgkmcnt(0)
	global_load_dword v112, v178, s[8:9]
	global_load_dword v120, v178, s[12:13]
	v_lshlrev_b32_e32 v2, 4, v0
	v_and_b32_e32 v2, 0x3f0, v2
	v_lshl_or_b32 v210, v1, 15, v2
	v_lshl_add_u64 v[94:95], s[6:7], 0, v[210:211]
	v_add_co_u32_e32 v42, vcc, s3, v94
	s_movk_i32 s9, 0x4000
	s_nop 0
	v_addc_co_u32_e32 v43, vcc, 0, v95, vcc
	v_add_co_u32_e32 v34, vcc, s14, v94
	s_mov_b32 s8, 0x800000
	s_nop 0
	v_addc_co_u32_e32 v35, vcc, 0, v95, vcc
	v_add_co_u32_e32 v66, vcc, s15, v94
	s_movk_i32 s3, 0x5000
	s_nop 0
	v_addc_co_u32_e32 v67, vcc, 0, v95, vcc
	v_add_co_u32_e32 v68, vcc, s9, v94
	v_lshrrev_b32_e32 v180, 5, v0
	s_nop 0
	v_addc_co_u32_e32 v69, vcc, 0, v95, vcc
	global_load_dwordx4 v[2:5], v[42:43], off offset:1024
	global_load_dwordx4 v[6:9], v[42:43], off offset:2048
	global_load_dwordx4 v[10:13], v[34:35], off offset:-4096
	global_load_dwordx4 v[14:17], v[34:35], off
	global_load_dwordx4 v[18:21], v[34:35], off offset:1024
	global_load_dwordx4 v[22:25], v[34:35], off offset:2048
	global_load_dwordx4 v[26:29], v[34:35], off offset:3072
	global_load_dwordx4 v[30:33], v[68:69], off offset:-4096
	v_and_b32_e32 v179, 31, v0
	v_lshlrev_b32_e32 v142, 5, v179
	s_waitcnt vmcnt(26)
	v_add_f32_e32 v34, 0, v36
	s_waitcnt vmcnt(25)
	v_add_f32_e32 v35, 0, v37
	s_waitcnt vmcnt(24)
	v_add_f32_e32 v34, v34, v38
	s_waitcnt vmcnt(23)
	v_add_f32_e32 v35, v35, v39
	s_waitcnt vmcnt(22)
	v_add_f32_e32 v34, v34, v40
	s_waitcnt vmcnt(21)
	v_add_f32_e32 v35, v35, v41
	s_waitcnt vmcnt(20)
	v_add_f32_e32 v34, v34, v44
	s_waitcnt vmcnt(19)
	v_add_f32_e32 v35, v35, v45
	s_waitcnt vmcnt(18)
	v_add_f32_e32 v34, v34, v46
	s_waitcnt vmcnt(17)
	v_add_f32_e32 v35, v35, v47
	s_waitcnt vmcnt(16)
	v_add_f32_e32 v34, v34, v48
	s_waitcnt vmcnt(15)
	v_add_f32_e32 v35, v35, v49
	s_waitcnt vmcnt(14)
	v_add_f32_e32 v34, v34, v50
	s_waitcnt vmcnt(13)
	v_add_f32_e32 v35, v35, v51
	s_waitcnt vmcnt(12)
	v_add_f32_e32 v44, v34, v52
	s_waitcnt vmcnt(11)
	v_add_f32_e32 v34, v35, v53
	v_mul_f32_e32 v35, 0x37a7c5ac, v44
	v_mul_f32_e32 v34, 0x37a7c5ac, v34
	v_fma_f32 v34, -v35, v35, v34
	v_add_f32_e32 v34, 0x3727c5ac, v34
	v_mul_f32_e32 v35, 0x4b800000, v34
	v_cmp_gt_f32_e32 vcc, s8, v34
	s_waitcnt vmcnt(9)
	v_fmamk_f32 v113, v44, 0x37a7c5ac, v112
	v_cndmask_b32_e32 v34, v34, v35, vcc
	v_rsq_f32_e32 v45, v34
	global_load_dwordx4 v[34:37], v[42:43], off offset:3072
	global_load_dwordx4 v[38:41], v[66:67], off offset:1024
	v_mul_f32_e32 v42, 0x45800000, v45
	v_cndmask_b32_e32 v42, v45, v42, vcc
	v_add_co_u32_e32 v110, vcc, s3, v94
	s_movk_i32 s3, 0x6000
	s_nop 0
	v_addc_co_u32_e32 v111, vcc, 0, v95, vcc
	v_add_co_u32_e32 v96, vcc, s3, v94
	s_movk_i32 s3, 0x7000
	s_nop 0
	v_addc_co_u32_e32 v97, vcc, 0, v95, vcc
	v_add_co_u32_e32 v118, vcc, s3, v94
	v_mul_f32_e32 v121, v42, v54
	global_load_dwordx4 v[42:45], v[66:67], off offset:2048
	global_load_dwordx4 v[46:49], v[66:67], off offset:3072
	global_load_dwordx4 v[50:53], v[68:69], off
	global_load_dwordx4 v[54:57], v[68:69], off offset:1024
	global_load_dwordx4 v[58:61], v[68:69], off offset:2048
	global_load_dwordx4 v[62:65], v[68:69], off offset:3072
	s_nop 0
	global_load_dwordx4 v[66:69], v[110:111], off offset:1024
	global_load_dwordx4 v[70:73], v[110:111], off offset:2048
	global_load_dwordx4 v[74:77], v[96:97], off offset:-4096
	global_load_dwordx4 v[78:81], v[96:97], off
	global_load_dwordx4 v[82:85], v[96:97], off offset:1024
	global_load_dwordx4 v[86:89], v[96:97], off offset:2048
	global_load_dwordx4 v[90:93], v[96:97], off offset:3072
	v_addc_co_u32_e32 v119, vcc, 0, v95, vcc
	global_load_dwordx4 v[94:97], v[110:111], off offset:3072
	global_load_dwordx4 v[98:101], v[118:119], off
	global_load_dwordx4 v[102:105], v[118:119], off offset:1024
	global_load_dwordx4 v[106:109], v[118:119], off offset:2048
	v_sub_f32_e32 v110, v112, v113
	s_waitcnt vmcnt(27)
	v_fmac_f32_e32 v120, v110, v121
	global_load_dwordx4 v[110:113], v210, s[6:7]
	global_load_dwordx4 v[114:117], v[118:119], off offset:3072
	ds_write2st64_b32 v178, v121, v120 offset1:4
	global_load_dwordx4 v[118:121], v210, s[6:7] offset:1024
	global_load_dwordx4 v[122:125], v210, s[6:7] offset:2048
	global_load_dwordx4 v[126:129], v210, s[6:7] offset:3072
	s_lshl_b32 s6, s2, 5
	v_or_b32_e32 v158, s6, v180
	v_min_i32_e32 v146, 0xc34f, v158
	v_ashrrev_i32_e32 v147, 31, v146
	v_lshlrev_b64 v[146:147], 9, v[146:147]
	v_lshl_add_u64 v[146:147], s[4:5], 0, v[146:147]
	v_lshlrev_b32_e32 v210, 4, v179
	v_lshl_add_u64 v[146:147], v[146:147], 0, v[210:211]
	s_waitcnt lgkmcnt(0)
	s_barrier
	ds_read_b128 v[130:133], v142
	ds_read_b128 v[134:137], v142 offset:16
	ds_read_b128 v[138:141], v142 offset:1024
	ds_read_b128 v[142:145], v142 offset:1040
	s_waitcnt lgkmcnt(0)
	s_barrier
	global_load_dwordx4 v[146:149], v[146:147], off nt
	v_or_b32_e32 v150, 8, v158
	v_min_i32_e32 v150, 0xc34f, v150
	v_ashrrev_i32_e32 v151, 31, v150
	v_lshlrev_b64 v[150:151], 9, v[150:151]
	v_lshl_add_u64 v[150:151], s[4:5], 0, v[150:151]
	v_lshl_add_u64 v[150:151], v[150:151], 0, v[210:211]
	global_load_dwordx4 v[150:153], v[150:151], off nt
	v_or_b32_e32 v154, 16, v158
	v_min_i32_e32 v154, 0xc34f, v154
	v_ashrrev_i32_e32 v155, 31, v154
	v_lshlrev_b64 v[154:155], 9, v[154:155]
	v_lshl_add_u64 v[154:155], s[4:5], 0, v[154:155]
	v_lshl_add_u64 v[154:155], v[154:155], 0, v[210:211]
	global_load_dwordx4 v[154:157], v[154:155], off nt
	v_or_b32_e32 v158, 24, v158
	v_min_i32_e32 v158, 0xc34f, v158
	v_ashrrev_i32_e32 v159, 31, v158
	v_lshlrev_b64 v[158:159], 9, v[158:159]
	v_lshl_add_u64 v[158:159], s[4:5], 0, v[158:159]
	v_lshl_add_u64 v[158:159], v[158:159], 0, v[210:211]
	global_load_dwordx4 v[158:161], v[158:159], off nt
	s_movk_i32 s7, 0x210
	v_mad_u32_u24 v216, v180, s7, v210
	s_mov_b32 s3, 0
	s_cmpk_gt_i32 s2, 0x61a
	s_waitcnt vmcnt(3)
	v_cvt_f32_f16_e32 v162, v146
	v_cvt_f32_f16_sdwa v163, v146 dst_sel:DWORD dst_unused:UNUSED_PAD src0_sel:WORD_1
	v_cvt_f32_f16_e32 v164, v147
	v_cvt_f32_f16_sdwa v165, v147 dst_sel:DWORD dst_unused:UNUSED_PAD src0_sel:WORD_1
	v_pk_fma_f32 v[162:163], v[130:131], v[162:163], v[138:139]
	s_nop 0
	v_max_f32_e32 v166, 0, v163
	v_max_f32_e32 v167, 0, v162
	v_pk_fma_f32 v[162:163], v[132:133], v[164:165], v[140:141]
	v_cvt_f32_f16_e32 v164, v148
	v_cvt_f32_f16_sdwa v165, v148 dst_sel:DWORD dst_unused:UNUSED_PAD src0_sel:WORD_1
	v_max_f32_e32 v168, 0, v162
	v_cvt_pk_f16_f32 v162, v167, v166
	v_cvt_f32_f16_e32 v166, v149
	v_cvt_f32_f16_sdwa v167, v149 dst_sel:DWORD dst_unused:UNUSED_PAD src0_sel:WORD_1
	v_pk_fma_f32 v[164:165], v[134:135], v[164:165], v[142:143]
	v_max_f32_e32 v163, 0, v163
	v_max_f32_e32 v165, 0, v165
	v_max_f32_e32 v164, 0, v164
	v_pk_fma_f32 v[166:167], v[136:137], v[166:167], v[144:145]
	v_cvt_pk_f16_f32 v164, v164, v165
	v_max_f32_e32 v165, 0, v167
	v_max_f32_e32 v166, 0, v166
	v_cvt_pk_f16_f32 v163, v168, v163
	v_cvt_pk_f16_f32 v165, v166, v165
	s_waitcnt vmcnt(2)
	v_cvt_f32_f16_e32 v166, v150
	v_cvt_f32_f16_sdwa v167, v150 dst_sel:DWORD dst_unused:UNUSED_PAD src0_sel:WORD_1
	ds_write_b128 v216, v[162:165]
	v_cvt_f32_f16_e32 v162, v151
	v_cvt_f32_f16_sdwa v163, v151 dst_sel:DWORD dst_unused:UNUSED_PAD src0_sel:WORD_1
	v_pk_fma_f32 v[164:165], v[130:131], v[166:167], v[138:139]
	v_pk_fma_f32 v[162:163], v[132:133], v[162:163], v[140:141]
	v_max_f32_e32 v166, 0, v165
	v_max_f32_e32 v167, 0, v164
	v_cvt_f32_f16_e32 v164, v152
	v_cvt_f32_f16_sdwa v165, v152 dst_sel:DWORD dst_unused:UNUSED_PAD src0_sel:WORD_1
	v_max_f32_e32 v168, 0, v162
	v_cvt_pk_f16_f32 v162, v167, v166
	v_cvt_f32_f16_e32 v166, v153
	v_cvt_f32_f16_sdwa v167, v153 dst_sel:DWORD dst_unused:UNUSED_PAD src0_sel:WORD_1
	v_pk_fma_f32 v[164:165], v[134:135], v[164:165], v[142:143]
	v_max_f32_e32 v163, 0, v163
	v_max_f32_e32 v165, 0, v165
	v_max_f32_e32 v164, 0, v164
	v_pk_fma_f32 v[166:167], v[136:137], v[166:167], v[144:145]
	v_cvt_pk_f16_f32 v164, v164, v165
	v_max_f32_e32 v165, 0, v167
	v_max_f32_e32 v166, 0, v166
	v_cvt_pk_f16_f32 v163, v168, v163
	v_cvt_pk_f16_f32 v165, v166, v165
	s_waitcnt vmcnt(1)
	v_cvt_f32_f16_e32 v166, v154
	v_cvt_f32_f16_sdwa v167, v154 dst_sel:DWORD dst_unused:UNUSED_PAD src0_sel:WORD_1
	ds_write_b128 v216, v[162:165] offset:4224
	v_cvt_f32_f16_e32 v162, v155
	v_cvt_f32_f16_sdwa v163, v155 dst_sel:DWORD dst_unused:UNUSED_PAD src0_sel:WORD_1
	v_pk_fma_f32 v[164:165], v[130:131], v[166:167], v[138:139]
	v_pk_fma_f32 v[162:163], v[132:133], v[162:163], v[140:141]
	v_max_f32_e32 v166, 0, v165
	v_max_f32_e32 v167, 0, v164
	v_cvt_f32_f16_e32 v164, v156
	v_cvt_f32_f16_sdwa v165, v156 dst_sel:DWORD dst_unused:UNUSED_PAD src0_sel:WORD_1
	v_max_f32_e32 v168, 0, v162
	v_cvt_pk_f16_f32 v162, v167, v166
	v_cvt_f32_f16_e32 v166, v157
	v_cvt_f32_f16_sdwa v167, v157 dst_sel:DWORD dst_unused:UNUSED_PAD src0_sel:WORD_1
	v_pk_fma_f32 v[164:165], v[134:135], v[164:165], v[142:143]
	v_max_f32_e32 v163, 0, v163
	v_max_f32_e32 v165, 0, v165
	v_max_f32_e32 v164, 0, v164
	v_pk_fma_f32 v[166:167], v[136:137], v[166:167], v[144:145]
	v_cvt_pk_f16_f32 v164, v164, v165
	v_max_f32_e32 v165, 0, v167
	v_max_f32_e32 v166, 0, v166
	v_cvt_pk_f16_f32 v163, v168, v163
	v_cvt_pk_f16_f32 v165, v166, v165
	s_waitcnt vmcnt(0)
	v_cvt_f32_f16_e32 v166, v158
	v_cvt_f32_f16_sdwa v167, v158 dst_sel:DWORD dst_unused:UNUSED_PAD src0_sel:WORD_1
	ds_write_b128 v216, v[162:165] offset:8448
	v_cvt_f32_f16_e32 v162, v159
	v_cvt_f32_f16_sdwa v163, v159 dst_sel:DWORD dst_unused:UNUSED_PAD src0_sel:WORD_1
	v_pk_fma_f32 v[164:165], v[130:131], v[166:167], v[138:139]
	v_pk_fma_f32 v[162:163], v[132:133], v[162:163], v[140:141]
	v_max_f32_e32 v166, 0, v165
	v_max_f32_e32 v167, 0, v164
	v_cvt_f32_f16_e32 v164, v160
	v_cvt_f32_f16_sdwa v165, v160 dst_sel:DWORD dst_unused:UNUSED_PAD src0_sel:WORD_1
	v_max_f32_e32 v168, 0, v162
	v_cvt_pk_f16_f32 v162, v167, v166
	v_cvt_f32_f16_e32 v166, v161
	v_cvt_f32_f16_sdwa v167, v161 dst_sel:DWORD dst_unused:UNUSED_PAD src0_sel:WORD_1
	v_pk_fma_f32 v[164:165], v[134:135], v[164:165], v[142:143]
	v_max_f32_e32 v163, 0, v163
	v_max_f32_e32 v165, 0, v165
	v_max_f32_e32 v164, 0, v164
	v_pk_fma_f32 v[166:167], v[136:137], v[166:167], v[144:145]
	v_cvt_pk_f16_f32 v164, v164, v165
	v_max_f32_e32 v165, 0, v167
	v_max_f32_e32 v166, 0, v166
	v_cvt_pk_f16_f32 v163, v168, v163
	v_cvt_pk_f16_f32 v165, v166, v165
	ds_write_b128 v216, v[162:165] offset:12672
	s_waitcnt lgkmcnt(0)
	s_barrier
	s_cbranch_scc1 .LBB3_11
	v_lshrrev_b32_e32 v162, 2, v0
	s_load_dwordx2 s[10:11], s[0:1], 0x10
	s_load_dword s12, s[0:1], 0x50
	s_load_dwordx2 s[8:9], s[0:1], 0x20
	v_and_b32_e32 v181, 12, v162
	s_movk_i32 s13, 0xc0
	v_and_or_b32 v162, v0, s13, v181
	v_lshlrev_b32_e32 v174, 2, v162
	s_waitcnt lgkmcnt(0)
	global_load_dwordx4 v[162:165], v174, s[10:11]
	global_load_dwordx4 v[166:169], v174, s[10:11] offset:64
	global_load_dwordx4 v[170:173], v174, s[10:11] offset:128
	s_nop 0
	global_load_dwordx4 v[174:177], v174, s[10:11] offset:192
	s_load_dwordx2 s[0:1], s[0:1], 0x40
	v_lshlrev_b32_e32 v179, 3, v179
	v_lshlrev_b32_e32 v210, 1, v179
	v_and_b32_e32 v182, 15, v0
	v_lshl_add_u64 v[212:213], s[4:5], 0, v[210:211]
	v_and_b32_e32 v179, 48, v0
	v_mul_u32_u24_e32 v210, 0xc350, v1
	v_lshlrev_b32_e32 v0, 1, v181
	s_waitcnt lgkmcnt(0)
	s_mov_b64 s[18:19], s[0:1]
	s_add_i32 s0, s2, s12
	v_and_b32_e32 v178, 0x300, v178
	v_lshl_or_b32 v218, s0, 5, v180
	s_lshl_b32 s0, s2, 15
	v_lshlrev_b32_e32 v180, 10, v182
	v_or3_b32 v178, s0, v180, v178
	s_movk_i32 s0, 0x40c0
	s_mov_b32 s11, 0x20000
	s_mov_b32 s10, 0x30d4000
	s_and_b32 s9, s9, 0xffff
	s_mov_b32 s13, 0xc350
	v_mad_u32_u24 v217, v182, s7, v179
	s_lshl_b32 s14, s12, 5
	v_add_u32_e32 v219, s6, v182
	v_or3_b32 v220, v178, v179, s0
	s_lshl_b32 s15, s12, 15
	s_mov_b32 s16, 0
	v_add_u32_e32 v210, v210, v219
	s_lshl_b32 s17, s12, 12
	v_lshl_add_u32 v210, v210, 7, v0
	s_waitcnt vmcnt(0)
	s_branch .LBB3_3
.LBB3_2:
	s_add_i32 s3, s3, s14
	s_andn2_b64 vcc, exec, s[0:1]
	v_add_u32_e32 v220, s15, v220
	v_add_u32_e32 v210, s17, v210
	s_waitcnt lgkmcnt(0)
	s_barrier
	s_cbranch_vccz .LBB3_11

.LBB3_5:
	global_load_dwordx2 v[242:243], v210, s[18:19]
	global_load_dwordx2 v[244:245], v210, s[18:19] offset:32
	global_load_dwordx2 v[246:247], v210, s[18:19] offset:64
	global_load_dwordx2 v[248:249], v210, s[18:19] offset:96
	global_load_dwordx2 v[250:251], v210, s[18:19] offset:2048
	global_load_dwordx2 v[252:253], v210, s[18:19] offset:2080
	global_load_dwordx2 v[254:255], v210, s[18:19] offset:2112
	global_load_dwordx2 v[0:1], v210, s[18:19] offset:2144
	s_mul_i32 s6, s16, 0x4200
	v_add_u32_e32 v214, s6, v217
	ds_read_b128 v[178:181], v214
	ds_read_b128 v[182:185], v214 offset:64
	ds_read_b128 v[198:201], v214 offset:8448
	ds_read_b128 v[202:205], v214 offset:8512
	s_waitcnt lgkmcnt(3)
	v_mfma_f32_16x16x32_f16 v[186:189], v[110:113], v[178:181], v[162:165]
	v_mfma_f32_16x16x32_f16 v[190:193], v[14:17], v[178:181], v[166:169]
	v_mfma_f32_16x16x32_f16 v[194:197], v[50:53], v[178:181], v[170:173]
	v_mfma_f32_16x16x32_f16 v[178:181], v[78:81], v[178:181], v[174:177]
	s_waitcnt lgkmcnt(1)
	v_mfma_f32_16x16x32_f16 v[206:209], v[110:113], v[198:201], v[162:165]
	v_mfma_f32_16x16x32_f16 v[222:225], v[14:17], v[198:201], v[166:169]
	v_mfma_f32_16x16x32_f16 v[226:229], v[50:53], v[198:201], v[170:173]
	v_mfma_f32_16x16x32_f16 v[198:201], v[78:81], v[198:201], v[174:177]
	v_mfma_f32_16x16x32_f16 v[186:189], v[118:121], v[182:185], v[186:189]
	v_mfma_f32_16x16x32_f16 v[190:193], v[18:21], v[182:185], v[190:193]
	v_mfma_f32_16x16x32_f16 v[194:197], v[54:57], v[182:185], v[194:197]
	v_mfma_f32_16x16x32_f16 v[178:181], v[82:85], v[182:185], v[178:181]
	s_waitcnt lgkmcnt(0)
	v_mfma_f32_16x16x32_f16 v[182:185], v[118:121], v[202:205], v[206:209]
	v_mfma_f32_16x16x32_f16 v[206:209], v[18:21], v[202:205], v[222:225]
	v_mfma_f32_16x16x32_f16 v[222:225], v[54:57], v[202:205], v[226:229]
	v_mfma_f32_16x16x32_f16 v[198:201], v[82:85], v[202:205], v[198:201]
	ds_read_b128 v[202:205], v214 offset:128
	s_nop 0
	ds_read_b128 v[226:229], v214 offset:192
	s_waitcnt lgkmcnt(1)
	v_mfma_f32_16x16x32_f16 v[186:189], v[122:125], v[202:205], v[186:189]
	v_mfma_f32_16x16x32_f16 v[190:193], v[22:25], v[202:205], v[190:193]
	v_mfma_f32_16x16x32_f16 v[194:197], v[58:61], v[202:205], v[194:197]
	v_mfma_f32_16x16x32_f16 v[178:181], v[86:89], v[202:205], v[178:181]
	ds_read_b128 v[202:205], v214 offset:8576
	ds_read_b128 v[230:233], v214 offset:8640
	s_waitcnt lgkmcnt(1)
	v_mfma_f32_16x16x32_f16 v[206:209], v[22:25], v[202:205], v[206:209]
	v_mfma_f32_16x16x32_f16 v[222:225], v[58:61], v[202:205], v[222:225]
	v_mfma_f32_16x16x32_f16 v[182:185], v[122:125], v[202:205], v[182:185]
	v_mfma_f32_16x16x32_f16 v[198:201], v[86:89], v[202:205], v[198:201]
	v_mfma_f32_16x16x32_f16 v[186:189], v[126:129], v[226:229], v[186:189]
	v_mfma_f32_16x16x32_f16 v[190:193], v[26:29], v[226:229], v[190:193]
	v_mfma_f32_16x16x32_f16 v[194:197], v[62:65], v[226:229], v[194:197]
	v_mfma_f32_16x16x32_f16 v[178:181], v[90:93], v[226:229], v[178:181]
	s_waitcnt lgkmcnt(0)
	v_mfma_f32_16x16x32_f16 v[202:205], v[26:29], v[230:233], v[206:209]
	v_mfma_f32_16x16x32_f16 v[206:209], v[62:65], v[230:233], v[222:225]
	s_nop 2
	ds_read_b128 v[222:225], v214 offset:256
	ds_read_b128 v[226:229], v214 offset:320
	v_mfma_f32_16x16x32_f16 v[182:185], v[126:129], v[230:233], v[182:185]
	v_mfma_f32_16x16x32_f16 v[198:201], v[90:93], v[230:233], v[198:201]
	s_waitcnt lgkmcnt(1)
	v_mfma_f32_16x16x32_f16 v[186:189], v[10:13], v[222:225], v[186:189]
	v_mfma_f32_16x16x32_f16 v[190:193], v[30:33], v[222:225], v[190:193]
	v_mfma_f32_16x16x32_f16 v[194:197], v[74:77], v[222:225], v[194:197]
	v_mfma_f32_16x16x32_f16 v[178:181], v[98:101], v[222:225], v[178:181]
	ds_read_b128 v[222:225], v214 offset:8704
	ds_read_b128 v[230:233], v214 offset:8768
	s_waitcnt lgkmcnt(1)
	v_mfma_f32_16x16x32_f16 v[182:185], v[10:13], v[222:225], v[182:185]
	v_mfma_f32_16x16x32_f16 v[202:205], v[30:33], v[222:225], v[202:205]
	v_mfma_f32_16x16x32_f16 v[206:209], v[74:77], v[222:225], v[206:209]
	v_mfma_f32_16x16x32_f16 v[198:201], v[98:101], v[222:225], v[198:201]
	v_mfma_f32_16x16x32_f16 v[186:189], v[2:5], v[226:229], v[186:189]
	v_mfma_f32_16x16x32_f16 v[190:193], v[38:41], v[226:229], v[190:193]
	v_mfma_f32_16x16x32_f16 v[194:197], v[66:69], v[226:229], v[194:197]
	v_mfma_f32_16x16x32_f16 v[178:181], v[102:105], v[226:229], v[178:181]
	ds_read_b128 v[222:225], v214 offset:384
	ds_read_b128 v[226:229], v214 offset:448
	s_waitcnt lgkmcnt(2)
	v_mfma_f32_16x16x32_f16 v[182:185], v[2:5], v[230:233], v[182:185]
	v_mfma_f32_16x16x32_f16 v[202:205], v[38:41], v[230:233], v[202:205]
	v_mfma_f32_16x16x32_f16 v[206:209], v[66:69], v[230:233], v[206:209]
	v_mfma_f32_16x16x32_f16 v[198:201], v[102:105], v[230:233], v[198:201]
	s_waitcnt lgkmcnt(1)
	v_mfma_f32_16x16x32_f16 v[186:189], v[6:9], v[222:225], v[186:189]
	v_mfma_f32_16x16x32_f16 v[190:193], v[42:45], v[222:225], v[190:193]
	v_mfma_f32_16x16x32_f16 v[194:197], v[70:73], v[222:225], v[194:197]
	v_mfma_f32_16x16x32_f16 v[178:181], v[106:109], v[222:225], v[178:181]
	ds_read_b128 v[222:225], v214 offset:8832
	ds_read_b128 v[230:233], v214 offset:8896
	v_add_u32_e32 v214, s3, v219
	v_cmp_gt_i32_e32 vcc, s13, v214
	s_waitcnt lgkmcnt(1)
	v_mfma_f32_16x16x32_f16 v[182:185], v[6:9], v[222:225], v[182:185]
	v_mfma_f32_16x16x32_f16 v[234:237], v[42:45], v[222:225], v[202:205]
	v_mfma_f32_16x16x32_f16 v[238:241], v[70:73], v[222:225], v[206:209]
	v_mfma_f32_16x16x32_f16 v[222:225], v[106:109], v[222:225], v[198:201]
	v_mfma_f32_16x16x32_f16 v[206:209], v[34:37], v[226:229], v[186:189]
	v_mfma_f32_16x16x32_f16 v[202:205], v[46:49], v[226:229], v[190:193]
	v_mfma_f32_16x16x32_f16 v[198:201], v[94:97], v[226:229], v[194:197]
	v_mfma_f32_16x16x32_f16 v[194:197], v[114:117], v[226:229], v[178:181]
	s_waitcnt lgkmcnt(0)
	v_mfma_f32_16x16x32_f16 v[190:193], v[34:37], v[230:233], v[182:185]
	v_mfma_f32_16x16x32_f16 v[186:189], v[46:49], v[230:233], v[234:237]
	v_mfma_f32_16x16x32_f16 v[182:185], v[94:97], v[230:233], v[238:241]
	v_mfma_f32_16x16x32_f16 v[178:181], v[114:117], v[230:233], v[222:225]
	s_and_saveexec_b64 s[6:7], vcc
	s_cbranch_execz .LBB3_7
	v_add_u32_e32 v215, 0xffffbf40, v220
	v_add_u32_e32 v221, 0xffffbf80, v220
	v_add_u32_e32 v238, 0xffffbfc0, v220
	v_add_u32_e32 v239, 0xffffc000, v220
	s_waitcnt vmcnt(4)
	v_cvt_f32_f16_e32 v230, v242
	v_cvt_f32_f16_sdwa v231, v242 dst_sel:DWORD dst_unused:UNUSED_PAD src0_sel:WORD_1
	v_cvt_f32_f16_e32 v224, v243
	v_cvt_f32_f16_sdwa v225, v243 dst_sel:DWORD dst_unused:UNUSED_PAD src0_sel:WORD_1
	v_cvt_f32_f16_e32 v232, v244
	v_cvt_f32_f16_sdwa v233, v244 dst_sel:DWORD dst_unused:UNUSED_PAD src0_sel:WORD_1
	v_cvt_f32_f16_e32 v226, v245
	v_cvt_f32_f16_sdwa v227, v245 dst_sel:DWORD dst_unused:UNUSED_PAD src0_sel:WORD_1
	v_cvt_f32_f16_e32 v234, v246
	v_cvt_f32_f16_sdwa v235, v246 dst_sel:DWORD dst_unused:UNUSED_PAD src0_sel:WORD_1
	v_cvt_f32_f16_e32 v228, v247
	v_cvt_f32_f16_sdwa v229, v247 dst_sel:DWORD dst_unused:UNUSED_PAD src0_sel:WORD_1
	v_cvt_f32_f16_e32 v236, v248
	v_cvt_f32_f16_sdwa v237, v248 dst_sel:DWORD dst_unused:UNUSED_PAD src0_sel:WORD_1
	v_cvt_f32_f16_e32 v222, v249
	v_cvt_f32_f16_sdwa v223, v249 dst_sel:DWORD dst_unused:UNUSED_PAD src0_sel:WORD_1
	v_pk_add_f32 v[208:209], v[208:209], v[224:225]
	v_pk_add_f32 v[206:207], v[206:207], v[230:231]
	v_pk_add_f32 v[204:205], v[204:205], v[226:227]
	v_pk_add_f32 v[202:203], v[202:203], v[232:233]
	v_pk_add_f32 v[200:201], v[200:201], v[228:229]
	v_pk_add_f32 v[198:199], v[198:199], v[234:235]
	v_pk_add_f32 v[196:197], v[196:197], v[222:223]
	v_pk_add_f32 v[194:195], v[194:195], v[236:237]
	buffer_store_dwordx4 v[206:209], v215, s[8:11], 0 offen sc1
	buffer_store_dwordx4 v[202:205], v221, s[8:11], 0 offen sc1
	buffer_store_dwordx4 v[198:201], v238, s[8:11], 0 offen sc1
	buffer_store_dwordx4 v[194:197], v239, s[8:11], 0 offen sc1
.LBB3_7:
	s_or_b64 exec, exec, s[6:7]
	s_nop 0
	v_add_u32_e32 v194, 16, v214
	v_cmp_gt_i32_e32 vcc, s13, v194
	s_and_saveexec_b64 s[6:7], vcc
	s_cbranch_execz .LBB3_9
	v_add_u32_e32 v214, 0xffffff40, v220
	v_add_u32_e32 v215, 0xffffff80, v220
	v_subrev_u32_e32 v221, 64, v220
	s_waitcnt vmcnt(4)
	v_cvt_f32_f16_e32 v202, v250
	v_cvt_f32_f16_sdwa v203, v250 dst_sel:DWORD dst_unused:UNUSED_PAD src0_sel:WORD_1
	v_cvt_f32_f16_e32 v196, v251
	v_cvt_f32_f16_sdwa v197, v251 dst_sel:DWORD dst_unused:UNUSED_PAD src0_sel:WORD_1
	v_cvt_f32_f16_e32 v204, v252
	v_cvt_f32_f16_sdwa v205, v252 dst_sel:DWORD dst_unused:UNUSED_PAD src0_sel:WORD_1
	v_cvt_f32_f16_e32 v198, v253
	v_cvt_f32_f16_sdwa v199, v253 dst_sel:DWORD dst_unused:UNUSED_PAD src0_sel:WORD_1
	v_cvt_f32_f16_e32 v206, v254
	v_cvt_f32_f16_sdwa v207, v254 dst_sel:DWORD dst_unused:UNUSED_PAD src0_sel:WORD_1
	v_cvt_f32_f16_e32 v200, v255
	v_cvt_f32_f16_sdwa v201, v255 dst_sel:DWORD dst_unused:UNUSED_PAD src0_sel:WORD_1
	v_cvt_f32_f16_e32 v208, v0
	v_cvt_f32_f16_sdwa v209, v0 dst_sel:DWORD dst_unused:UNUSED_PAD src0_sel:WORD_1
	v_cvt_f32_f16_e32 v194, v1
	v_cvt_f32_f16_sdwa v195, v1 dst_sel:DWORD dst_unused:UNUSED_PAD src0_sel:WORD_1
	v_pk_add_f32 v[192:193], v[192:193], v[196:197]
	v_pk_add_f32 v[190:191], v[190:191], v[202:203]
	v_pk_add_f32 v[188:189], v[188:189], v[198:199]
	v_pk_add_f32 v[186:187], v[186:187], v[204:205]
	v_pk_add_f32 v[184:185], v[184:185], v[200:201]
	v_pk_add_f32 v[182:183], v[182:183], v[206:207]
	v_pk_add_f32 v[180:181], v[180:181], v[194:195]
	v_pk_add_f32 v[178:179], v[178:179], v[208:209]
	buffer_store_dwordx4 v[190:193], v214, s[8:11], 0 offen sc1
	buffer_store_dwordx4 v[186:189], v215, s[8:11], 0 offen sc1
	buffer_store_dwordx4 v[182:185], v221, s[8:11], 0 offen sc1
	buffer_store_dwordx4 v[178:181], v220, s[8:11], 0 offen sc1
.LBB3_9:
	s_or_b64 exec, exec, s[6:7]
	s_andn2_b64 vcc, exec, s[4:5]
	s_xor_b32 s16, s16, 1
	s_cbranch_vccnz .LBB3_2
	s_waitcnt vmcnt(8)
	v_cvt_f32_f16_sdwa v179, v146 dst_sel:DWORD dst_unused:UNUSED_PAD src0_sel:WORD_1
	v_cvt_f32_f16_e32 v178, v146
	v_cvt_f32_f16_sdwa v181, v147 dst_sel:DWORD dst_unused:UNUSED_PAD src0_sel:WORD_1
	v_cvt_f32_f16_e32 v180, v147
	v_cvt_f32_f16_sdwa v183, v148 dst_sel:DWORD dst_unused:UNUSED_PAD src0_sel:WORD_1
	v_cvt_f32_f16_e32 v182, v148
	v_pk_fma_f32 v[178:179], v[130:131], v[178:179], v[138:139]
	v_pk_fma_f32 v[180:181], v[132:133], v[180:181], v[140:141]
	v_max_f32_e32 v179, 0, v179
	v_max_f32_e32 v178, 0, v178
	v_cvt_pk_f16_f32 v178, v178, v179
	v_max_f32_e32 v179, 0, v181
	v_max_f32_e32 v180, 0, v180
	v_cvt_pk_f16_f32 v179, v180, v179
	v_pk_fma_f32 v[180:181], v[134:135], v[182:183], v[142:143]
	v_cvt_f32_f16_sdwa v183, v149 dst_sel:DWORD dst_unused:UNUSED_PAD src0_sel:WORD_1
	v_cvt_f32_f16_e32 v182, v149
	v_max_f32_e32 v181, 0, v181
	v_max_f32_e32 v180, 0, v180
	v_cvt_pk_f16_f32 v180, v180, v181
	v_pk_fma_f32 v[182:183], v[136:137], v[182:183], v[144:145]
	s_mul_i32 s4, s16, 0x4200
	v_max_f32_e32 v181, 0, v183
	v_max_f32_e32 v182, 0, v182
	v_cvt_pk_f16_f32 v181, v182, v181
	v_cvt_f32_f16_sdwa v183, v150 dst_sel:DWORD dst_unused:UNUSED_PAD src0_sel:WORD_1
	v_cvt_f32_f16_e32 v182, v150
	v_add_u32_e32 v186, s4, v216
	ds_write_b128 v186, v[178:181]
	v_cvt_f32_f16_sdwa v181, v151 dst_sel:DWORD dst_unused:UNUSED_PAD src0_sel:WORD_1
	v_cvt_f32_f16_e32 v180, v151
	v_pk_fma_f32 v[178:179], v[130:131], v[182:183], v[138:139]
	v_cvt_f32_f16_sdwa v183, v152 dst_sel:DWORD dst_unused:UNUSED_PAD src0_sel:WORD_1
	v_cvt_f32_f16_e32 v182, v152
	v_max_f32_e32 v179, 0, v179
	v_max_f32_e32 v178, 0, v178
	v_pk_fma_f32 v[180:181], v[132:133], v[180:181], v[140:141]
	v_cvt_pk_f16_f32 v178, v178, v179
	v_max_f32_e32 v179, 0, v181
	v_max_f32_e32 v180, 0, v180
	v_cvt_pk_f16_f32 v179, v180, v179
	v_pk_fma_f32 v[180:181], v[134:135], v[182:183], v[142:143]
	v_cvt_f32_f16_sdwa v183, v153 dst_sel:DWORD dst_unused:UNUSED_PAD src0_sel:WORD_1
	v_cvt_f32_f16_e32 v182, v153
	v_max_f32_e32 v181, 0, v181
	v_max_f32_e32 v180, 0, v180
	v_cvt_pk_f16_f32 v180, v180, v181
	v_pk_fma_f32 v[182:183], v[136:137], v[182:183], v[144:145]
	v_cvt_f32_f16_sdwa v185, v154 dst_sel:DWORD dst_unused:UNUSED_PAD src0_sel:WORD_1
	v_max_f32_e32 v181, 0, v183
	v_max_f32_e32 v182, 0, v182
	v_cvt_f32_f16_e32 v184, v154
	v_cvt_pk_f16_f32 v181, v182, v181
	ds_write_b128 v186, v[178:181] offset:4224
	v_cvt_f32_f16_sdwa v181, v155 dst_sel:DWORD dst_unused:UNUSED_PAD src0_sel:WORD_1
	v_cvt_f32_f16_e32 v180, v155
	v_cvt_f32_f16_sdwa v183, v156 dst_sel:DWORD dst_unused:UNUSED_PAD src0_sel:WORD_1
	v_cvt_f32_f16_e32 v182, v156
	v_pk_fma_f32 v[178:179], v[130:131], v[184:185], v[138:139]
	v_pk_fma_f32 v[180:181], v[132:133], v[180:181], v[140:141]
	v_max_f32_e32 v179, 0, v179
	v_max_f32_e32 v178, 0, v178
	v_cvt_pk_f16_f32 v178, v178, v179
	v_max_f32_e32 v179, 0, v181
	v_max_f32_e32 v180, 0, v180
	v_cvt_pk_f16_f32 v179, v180, v179
	v_pk_fma_f32 v[180:181], v[134:135], v[182:183], v[142:143]
	v_cvt_f32_f16_sdwa v183, v157 dst_sel:DWORD dst_unused:UNUSED_PAD src0_sel:WORD_1
	v_cvt_f32_f16_e32 v182, v157
	v_max_f32_e32 v181, 0, v181
	v_max_f32_e32 v180, 0, v180
	v_cvt_pk_f16_f32 v180, v180, v181
	v_pk_fma_f32 v[182:183], v[136:137], v[182:183], v[144:145]
	v_cvt_f32_f16_sdwa v185, v158 dst_sel:DWORD dst_unused:UNUSED_PAD src0_sel:WORD_1
	v_max_f32_e32 v181, 0, v183
	v_max_f32_e32 v182, 0, v182
	v_cvt_f32_f16_e32 v184, v158
	v_cvt_pk_f16_f32 v181, v182, v181
	ds_write_b128 v186, v[178:181] offset:8448
	v_cvt_f32_f16_sdwa v181, v159 dst_sel:DWORD dst_unused:UNUSED_PAD src0_sel:WORD_1
	v_cvt_f32_f16_e32 v180, v159
	v_cvt_f32_f16_sdwa v183, v160 dst_sel:DWORD dst_unused:UNUSED_PAD src0_sel:WORD_1
	v_cvt_f32_f16_e32 v182, v160
	v_pk_fma_f32 v[178:179], v[130:131], v[184:185], v[138:139]
	v_pk_fma_f32 v[180:181], v[132:133], v[180:181], v[140:141]
	v_max_f32_e32 v179, 0, v179
	v_max_f32_e32 v178, 0, v178
	v_cvt_pk_f16_f32 v178, v178, v179
	v_max_f32_e32 v179, 0, v181
	v_max_f32_e32 v180, 0, v180
	v_cvt_pk_f16_f32 v179, v180, v179
	v_pk_fma_f32 v[180:181], v[134:135], v[182:183], v[142:143]
	v_cvt_f32_f16_sdwa v183, v161 dst_sel:DWORD dst_unused:UNUSED_PAD src0_sel:WORD_1
	v_cvt_f32_f16_e32 v182, v161
	v_max_f32_e32 v181, 0, v181
	v_max_f32_e32 v180, 0, v180
	v_cvt_pk_f16_f32 v180, v180, v181
	v_pk_fma_f32 v[182:183], v[136:137], v[182:183], v[144:145]
	s_nop 0
	v_max_f32_e32 v181, 0, v183
	v_max_f32_e32 v182, 0, v182
	v_cvt_pk_f16_f32 v181, v182, v181
	ds_write_b128 v186, v[178:181] offset:12672
	s_branch .LBB3_2

	.amdhsa_kernel _Z11gemm_kernelILi2EEvPKDF16_S1_PKfPDF16_PfS5_S3_S3_S1_S3_
		.amdhsa_group_segment_fixed_size 33792
		.amdhsa_private_segment_fixed_size 0
		.amdhsa_kernarg_size 336
		.amdhsa_user_sgpr_count 2
		.amdhsa_user_sgpr_dispatch_ptr 0
		.amdhsa_user_sgpr_queue_ptr 0
		.amdhsa_user_sgpr_kernarg_segment_ptr 1
		.amdhsa_user_sgpr_dispatch_id 0
		.amdhsa_user_sgpr_kernarg_preload_length 0
		.amdhsa_user_sgpr_kernarg_preload_offset 0
		.amdhsa_user_sgpr_private_segment_size 0
		.amdhsa_uses_dynamic_stack 0
		.amdhsa_enable_private_segment 0
		.amdhsa_system_sgpr_workgroup_id_x 1
		.amdhsa_system_sgpr_workgroup_id_y 0
		.amdhsa_system_sgpr_workgroup_id_z 0
		.amdhsa_system_sgpr_workgroup_info 0
		.amdhsa_system_vgpr_workitem_id 0
		.amdhsa_next_free_vgpr 256
		.amdhsa_next_free_sgpr 96
		.amdhsa_accum_offset 256
		.amdhsa_reserve_vcc 1
		.amdhsa_float_round_mode_32 0
		.amdhsa_float_round_mode_16_64 0
		.amdhsa_float_denorm_mode_32 3
		.amdhsa_float_denorm_mode_16_64 3
		.amdhsa_dx10_clamp 1
		.amdhsa_ieee_mode 1
		.amdhsa_fp16_overflow 0
		.amdhsa_tg_split 0
		.amdhsa_exception_fp_ieee_invalid_op 0
		.amdhsa_exception_fp_denorm_src 0
		.amdhsa_exception_fp_ieee_div_zero 0
		.amdhsa_exception_fp_ieee_overflow 0
		.amdhsa_exception_fp_ieee_underflow 0
		.amdhsa_exception_fp_ieee_inexact 0
		.amdhsa_exception_int_div_zero 0
	.end_amdhsa_kernel

	.text
	.p2alignl 8, 3212836864
	.fill 256, 4, 3212836864

amdhsa.kernels:
  - .agpr_count:     0
    .args:
      - .actual_access:  read_only
        .address_space:  global
        .offset:         0
        .size:           8
        .value_kind:     global_buffer
      - .actual_access:  read_only
        .address_space:  global
        .offset:         8
        .size:           8
        .value_kind:     global_buffer
      - .actual_access:  read_only
        .address_space:  global
        .offset:         16
        .size:           8
        .value_kind:     global_buffer
      - .actual_access:  read_only
        .address_space:  global
        .offset:         24
        .size:           8
        .value_kind:     global_buffer
      - .actual_access:  read_only
        .address_space:  global
        .offset:         32
        .size:           8
        .value_kind:     global_buffer
      - .address_space:  global
        .offset:         40
        .size:           8
        .value_kind:     global_buffer
      - .actual_access:  write_only
        .address_space:  global
        .offset:         48
        .size:           8
        .value_kind:     global_buffer
      - .actual_access:  write_only
        .address_space:  global
        .offset:         56
        .size:           8
        .value_kind:     global_buffer
      - .actual_access:  write_only
        .address_space:  global
        .offset:         64
        .size:           8
        .value_kind:     global_buffer
      - .actual_access:  write_only
        .address_space:  global
        .offset:         72
        .size:           8
        .value_kind:     global_buffer
      - .actual_access:  write_only
        .address_space:  global
        .offset:         80
        .size:           8
        .value_kind:     global_buffer
    .group_segment_fixed_size: 3132
    .kernarg_segment_align: 8
    .kernarg_segment_size: 88
    .language:       OpenCL C
    .language_version:
      - 2
      - 0
    .max_flat_workgroup_size: 256
    .name:           _Z11prep_kernelPKfPKiS0_S0_S0_PiP15HIP_vector_typeIjLj2EEP6OvfRecPDF16_S9_S9_
    .private_segment_fixed_size: 0
    .sgpr_count:     38
    .sgpr_spill_count: 0
    .symbol:         _Z11prep_kernelPKfPKiS0_S0_S0_PiP15HIP_vector_typeIjLj2EEP6OvfRecPDF16_S9_S9_.kd
    .uniform_work_group_size: 1
    .uses_dynamic_stack: false
    .vgpr_count:     42
    .vgpr_spill_count: 0
    .wavefront_size: 64
  - .agpr_count:     0
    .args:
      - .actual_access:  read_only
        .address_space:  global
        .offset:         0
        .size:           8
        .value_kind:     global_buffer
      - .actual_access:  read_only
        .address_space:  global
        .offset:         8
        .size:           8
        .value_kind:     global_buffer
      - .actual_access:  read_only
        .address_space:  global
        .offset:         16
        .size:           8
        .value_kind:     global_buffer
      - .address_space:  global
        .offset:         24
        .size:           8
        .value_kind:     global_buffer
      - .actual_access:  read_only
        .address_space:  global
        .offset:         32
        .size:           8
        .value_kind:     global_buffer
      - .actual_access:  write_only
        .address_space:  global
        .offset:         40
        .size:           8
        .value_kind:     global_buffer
    .group_segment_fixed_size: 12112
    .kernarg_segment_align: 8
    .kernarg_segment_size: 48
    .language:       OpenCL C
    .language_version:
      - 2
      - 0
    .max_flat_workgroup_size: 256
    .name:           _Z13gather_kernelPK15HIP_vector_typeIjLj2EEPKiPK6OvfRecPKDF16_PKfPDF16_
    .private_segment_fixed_size: 0
    .sgpr_count:     41
    .sgpr_spill_count: 0
    .symbol:         _Z13gather_kernelPK15HIP_vector_typeIjLj2EEPKiPK6OvfRecPKDF16_PKfPDF16_.kd
    .uniform_work_group_size: 1
    .uses_dynamic_stack: false
    .vgpr_count:     63
    .vgpr_spill_count: 0
    .wavefront_size: 64
  - .agpr_count:     0
    .args:
      - .actual_access:  read_only
        .address_space:  global
        .offset:         0
        .size:           8
        .value_kind:     global_buffer
      - .actual_access:  read_only
        .address_space:  global
        .offset:         8
        .size:           8
        .value_kind:     global_buffer
      - .actual_access:  read_only
        .address_space:  global
        .offset:         16
        .size:           8
        .value_kind:     global_buffer
      - .actual_access:  write_only
        .address_space:  global
        .offset:         24
        .size:           8
        .value_kind:     global_buffer
      - .actual_access:  read_only
        .address_space:  global
        .offset:         32
        .size:           8
        .value_kind:     global_buffer
      - .address_space:  global
        .offset:         40
        .size:           8
        .value_kind:     global_buffer
      - .actual_access:  read_only
        .address_space:  global
        .offset:         48
        .size:           8
        .value_kind:     global_buffer
      - .actual_access:  read_only
        .address_space:  global
        .offset:         56
        .size:           8
        .value_kind:     global_buffer
      - .actual_access:  read_only
        .address_space:  global
        .offset:         64
        .size:           8
        .value_kind:     global_buffer
      - .actual_access:  read_only
        .address_space:  global
        .offset:         72
        .size:           8
        .value_kind:     global_buffer
      - .offset:         80
        .size:           4
        .value_kind:     hidden_block_count_x
      - .offset:         84
        .size:           4
        .value_kind:     hidden_block_count_y
      - .offset:         88
        .size:           4
        .value_kind:     hidden_block_count_z
      - .offset:         92
        .size:           2
        .value_kind:     hidden_group_size_x
      - .offset:         94
        .size:           2
        .value_kind:     hidden_group_size_y
      - .offset:         96
        .size:           2
        .value_kind:     hidden_group_size_z
      - .offset:         98
        .size:           2
        .value_kind:     hidden_remainder_x
      - .offset:         100
        .size:           2
        .value_kind:     hidden_remainder_y
      - .offset:         102
        .size:           2
        .value_kind:     hidden_remainder_z
      - .offset:         120
        .size:           8
        .value_kind:     hidden_global_offset_x
      - .offset:         128
        .size:           8
        .value_kind:     hidden_global_offset_y
      - .offset:         136
        .size:           8
        .value_kind:     hidden_global_offset_z
      - .offset:         144
        .size:           2
        .value_kind:     hidden_grid_dims
    .group_segment_fixed_size: 33792
    .kernarg_segment_align: 8
    .kernarg_segment_size: 336
    .language:       OpenCL C
    .language_version:
      - 2
      - 0
    .max_flat_workgroup_size: 256
    .name:           _Z11gemm_kernelILi1EEvPKDF16_S1_PKfPDF16_PfS5_S3_S3_S1_S3_
    .private_segment_fixed_size: 0
    .sgpr_count:     27
    .sgpr_spill_count: 0
    .symbol:         _Z11gemm_kernelILi1EEvPKDF16_S1_PKfPDF16_PfS5_S3_S3_S1_S3_.kd
    .uniform_work_group_size: 1
    .uses_dynamic_stack: false
    .vgpr_count:     240
    .vgpr_spill_count: 0
    .wavefront_size: 64
  - .agpr_count:     0
    .args:
      - .actual_access:  read_only
        .address_space:  global
        .offset:         0
        .size:           8
        .value_kind:     global_buffer
      - .actual_access:  read_only
        .address_space:  global
        .offset:         8
        .size:           8
        .value_kind:     global_buffer
      - .actual_access:  read_only
        .address_space:  global
        .offset:         16
        .size:           8
        .value_kind:     global_buffer
      - .actual_access:  read_only
        .address_space:  global
        .offset:         24
        .size:           8
        .value_kind:     global_buffer
      - .actual_access:  write_only
        .address_space:  global
        .offset:         32
        .size:           8
        .value_kind:     global_buffer
      - .actual_access:  read_only
        .address_space:  global
        .offset:         40
        .size:           8
        .value_kind:     global_buffer
      - .actual_access:  read_only
        .address_space:  global
        .offset:         48
        .size:           8
        .value_kind:     global_buffer
      - .actual_access:  read_only
        .address_space:  global
        .offset:         56
        .size:           8
        .value_kind:     global_buffer
      - .actual_access:  read_only
        .address_space:  global
        .offset:         64
        .size:           8
        .value_kind:     global_buffer
      - .actual_access:  read_only
        .address_space:  global
        .offset:         72
        .size:           8
        .value_kind:     global_buffer
      - .offset:         80
        .size:           4
        .value_kind:     hidden_block_count_x
      - .offset:         84
        .size:           4
        .value_kind:     hidden_block_count_y
      - .offset:         88
        .size:           4
        .value_kind:     hidden_block_count_z
      - .offset:         92
        .size:           2
        .value_kind:     hidden_group_size_x
      - .offset:         94
        .size:           2
        .value_kind:     hidden_group_size_y
      - .offset:         96
        .size:           2
        .value_kind:     hidden_group_size_z
      - .offset:         98
        .size:           2
        .value_kind:     hidden_remainder_x
      - .offset:         100
        .size:           2
        .value_kind:     hidden_remainder_y
      - .offset:         102
        .size:           2
        .value_kind:     hidden_remainder_z
      - .offset:         120
        .size:           8
        .value_kind:     hidden_global_offset_x
      - .offset:         128
        .size:           8
        .value_kind:     hidden_global_offset_y
      - .offset:         136
        .size:           8
        .value_kind:     hidden_global_offset_z
      - .offset:         144
        .size:           2
        .value_kind:     hidden_grid_dims
    .group_segment_fixed_size: 33792
    .kernarg_segment_align: 8
    .kernarg_segment_size: 336
    .language:       OpenCL C
    .language_version:
      - 2
      - 0
    .max_flat_workgroup_size: 256
    .name:           _Z11gemm_kernelILi2EEvPKDF16_S1_PKfPDF16_PfS5_S3_S3_S1_S3_
    .private_segment_fixed_size: 0
    .sgpr_count:     23
    .sgpr_spill_count: 0
    .symbol:         _Z11gemm_kernelILi2EEvPKDF16_S1_PKfPDF16_PfS5_S3_S3_S1_S3_.kd
    .uniform_work_group_size: 1
    .uses_dynamic_stack: false
    .vgpr_count:     256
    .vgpr_spill_count: 0
    .wavefront_size: 64
